# baseline (speedup 1.0000x reference)
.Lpoll_done_0:
	ds_read_b128 v[142:145], v202 offset:58112
	ds_read_b128 v[146:149], v202 offset:58176
	v_mul_f32_e32 v176, v166, v152
	v_mul_f32_e32 v177, v167, v153
	v_mul_f32_e32 v240, v116, v150
	v_mul_f32_e32 v241, v117, v151
	s_waitcnt lgkmcnt(1)
	v_mfma_f32_16x16x32_bf16 v[134:137], v[134:137], v[142:145], 0
	v_add_f32_e64 v242, -v116, 1.0
	v_add_f32_e64 v243, -v117, 1.0
	s_waitcnt lgkmcnt(0)
	v_sub_f32_e32 v144, 1.0, v236
	v_sub_f32_e32 v145, 1.0, v237
	v_mfma_f32_16x16x32_bf16 v[140:143], v[138:141], v[146:149], 0
	v_sub_f32_e32 v154, 1.0, v238
	v_sub_f32_e32 v155, 1.0, v239
	v_sub_f32_e32 v156, 1.0, v166
	v_sub_f32_e32 v157, 1.0, v167
	v_sub_f32_e32 v158, v150, v174
	v_sub_f32_e32 v159, v151, v175
	v_sub_f32_e32 v160, v152, v172
	v_sub_f32_e32 v161, v153, v173
	v_add_f32_e32 v138, v136, v142
	v_add_f32_e32 v139, v137, v143
	v_add_f32_e32 v142, v134, v140
	v_add_f32_e32 v143, v135, v141
	v_mul_f32_e32 v136, v238, v138
	v_mul_f32_e32 v137, v239, v139
	v_mul_f32_e32 v134, v236, v142
	v_mul_f32_e32 v135, v237, v143
	v_fma_f32 v144, v174, v144, v134
	v_fma_f32 v145, v175, v145, v135
	v_fma_f32 v140, v172, v154, v136
	v_fma_f32 v141, v173, v155, v137
	v_fma_f32 v134, v242, v144, v240
	v_fma_f32 v135, v243, v145, v241
	v_fma_f32 v136, v156, v140, v176
	v_fma_f32 v137, v157, v141, v177
	s_and_saveexec_b64 s[42:43], s[16:17]
	s_cbranch_execz .LBB1_71
	v_mov_b32_e32 v115, s56
	v_cndmask_b32_e64 v115, v137, v115, s[14:15]
	v_cndmask_b32_e64 v147, v136, v136, s[14:15]
	v_cndmask_b32_e64 v146, v135, v135, s[14:15]
	v_cndmask_b32_e64 v148, v134, v134, s[14:15]
	v_cvt_pk_bf16_f32 v146, v148, v146
	v_cvt_pk_bf16_f32 v147, v147, v115
	v_mad_u32_u24 v115, v233, s53, v204
	ds_write_b64 v115, v[146:147]

.LBB1_77:
	s_or_b64 exec, exec, s[42:43]
	v_sub_f32_e32 v134, v150, v142
	v_add_f32_e64 v115, |v158|, |v134|
	v_sub_f32_e32 v134, v150, v144
	v_add_f32_e64 v115, v115, |v134|
	v_sub_f32_e32 v135, v151, v143
	v_add_f32_e64 v134, |v159|, |v135|
	v_sub_f32_e32 v135, v151, v145
	v_fma_f32 v115, v116, v115, 0
	v_add_f32_e32 v116, 0, v116
	v_add_f32_e64 v134, v134, |v135|
	v_fmac_f32_e32 v115, v117, v134
	v_add_f32_e32 v116, v117, v116
	v_sub_f32_e32 v134, v152, v138
	v_add_f32_e64 v117, |v160|, |v134|
	v_sub_f32_e32 v134, v152, v140
	v_add_f32_e64 v117, v117, |v134|
	v_fmac_f32_e32 v115, v166, v117
	v_sub_f32_e32 v134, v153, v139
	v_add_f32_e64 v117, |v161|, |v134|
	v_sub_f32_e32 v134, v153, v141
	v_add_f32_e64 v117, v117, |v134|
	v_fmac_f32_e32 v115, v167, v117
	v_add_f32_e32 v116, v166, v116
	v_add_f32_e32 v116, v167, v116
	v_mov_b32_e32 v246, v115
	v_mov_b32_e32 v247, v116

.Lpoll_done_1:
	ds_read_b128 v[142:145], v202 offset:58112
	ds_read_b128 v[146:149], v202 offset:58176
	v_mul_f32_e32 v240, v172, v152
	v_mul_f32_e32 v241, v173, v153
	v_mul_f32_e32 v242, v116, v150
	v_mul_f32_e32 v243, v117, v151
	s_waitcnt lgkmcnt(1)
	v_mfma_f32_16x16x32_bf16 v[134:137], v[134:137], v[142:145], 0
	v_add_f32_e64 v244, -v116, 1.0
	v_add_f32_e64 v245, -v117, 1.0
	s_waitcnt lgkmcnt(0)
	v_sub_f32_e32 v144, 1.0, v236
	v_sub_f32_e32 v145, 1.0, v237
	v_mfma_f32_16x16x32_bf16 v[140:143], v[138:141], v[146:149], 0
	v_sub_f32_e32 v154, 1.0, v238
	v_sub_f32_e32 v155, 1.0, v239
	v_sub_f32_e32 v156, 1.0, v172
	v_sub_f32_e32 v157, 1.0, v173
	v_sub_f32_e32 v158, v150, v176
	v_sub_f32_e32 v159, v151, v177
	v_sub_f32_e32 v160, v152, v174
	v_sub_f32_e32 v161, v153, v175
	v_add_f32_e32 v138, v136, v142
	v_add_f32_e32 v139, v137, v143
	v_add_f32_e32 v142, v134, v140
	v_add_f32_e32 v143, v135, v141
	v_mul_f32_e32 v136, v238, v138
	v_mul_f32_e32 v137, v239, v139
	v_mul_f32_e32 v134, v236, v142
	v_mul_f32_e32 v135, v237, v143
	v_fma_f32 v144, v176, v144, v134
	v_fma_f32 v145, v177, v145, v135
	v_fma_f32 v140, v174, v154, v136
	v_fma_f32 v141, v175, v155, v137
	v_fma_f32 v134, v244, v144, v242
	v_fma_f32 v135, v245, v145, v243
	v_fma_f32 v136, v156, v140, v240
	v_fma_f32 v137, v157, v141, v241
	s_and_saveexec_b64 s[42:43], s[16:17]
	s_cbranch_execz .LBB1_107
	v_mov_b32_e32 v115, s56
	v_cndmask_b32_e64 v115, v137, v115, s[14:15]
	v_cndmask_b32_e64 v147, v136, v136, s[14:15]
	v_cndmask_b32_e64 v146, v135, v135, s[14:15]
	v_cndmask_b32_e64 v148, v134, v134, s[14:15]
	v_cvt_pk_bf16_f32 v146, v148, v146
	v_cvt_pk_bf16_f32 v147, v147, v115
	v_mad_u32_u24 v115, v167, s53, v204
	ds_write_b64 v115, v[146:147]

.LBB1_113:
	s_or_b64 exec, exec, s[42:43]
	v_sub_f32_e32 v134, v150, v142
	v_add_f32_e64 v115, |v158|, |v134|
	v_sub_f32_e32 v134, v150, v144
	v_add_f32_e64 v115, v115, |v134|
	v_sub_f32_e32 v135, v151, v143
	v_add_f32_e64 v134, |v159|, |v135|
	v_sub_f32_e32 v135, v151, v145
	v_fma_f32 v115, v116, v115, 0
	v_add_f32_e32 v116, 0, v116
	v_add_f32_e64 v134, v134, |v135|
	v_fmac_f32_e32 v115, v117, v134
	v_add_f32_e32 v116, v117, v116
	v_sub_f32_e32 v134, v152, v138
	v_add_f32_e64 v117, |v160|, |v134|
	v_sub_f32_e32 v134, v152, v140
	v_add_f32_e64 v117, v117, |v134|
	v_fmac_f32_e32 v115, v172, v117
	v_sub_f32_e32 v134, v153, v139
	v_add_f32_e64 v117, |v161|, |v134|
	v_sub_f32_e32 v134, v153, v141
	v_add_f32_e64 v117, v117, |v134|
	v_fmac_f32_e32 v115, v173, v117
	v_add_f32_e32 v116, v172, v116
	v_add_f32_e32 v116, v173, v116
	v_mov_b32_e32 v246, v115
	v_mov_b32_e32 v247, v116

.Lpoll_done_2:
	ds_read_b128 v[142:145], v202 offset:58112
	ds_read_b128 v[146:149], v202 offset:58176
	v_mul_f32_e32 v242, v172, v152
	v_mul_f32_e32 v243, v173, v153
	v_mul_f32_e32 v244, v116, v150
	v_mul_f32_e32 v245, v117, v151
	s_waitcnt lgkmcnt(1)
	v_mfma_f32_16x16x32_bf16 v[134:137], v[134:137], v[142:145], 0
	v_add_f32_e64 v246, -v116, 1.0
	v_add_f32_e64 v247, -v117, 1.0
	s_waitcnt lgkmcnt(0)
	v_sub_f32_e32 v144, 1.0, v238
	v_sub_f32_e32 v145, 1.0, v239
	v_mfma_f32_16x16x32_bf16 v[140:143], v[138:141], v[146:149], 0
	v_sub_f32_e32 v154, 1.0, v240
	v_sub_f32_e32 v155, 1.0, v241
	v_sub_f32_e32 v156, 1.0, v172
	v_sub_f32_e32 v157, 1.0, v173
	v_sub_f32_e32 v158, v150, v176
	v_sub_f32_e32 v159, v151, v177
	v_sub_f32_e32 v160, v152, v174
	v_sub_f32_e32 v161, v153, v175
	v_add_f32_e32 v138, v136, v142
	v_add_f32_e32 v139, v137, v143
	v_add_f32_e32 v142, v134, v140
	v_add_f32_e32 v143, v135, v141
	v_mul_f32_e32 v136, v240, v138
	v_mul_f32_e32 v137, v241, v139
	v_mul_f32_e32 v134, v238, v142
	v_mul_f32_e32 v135, v239, v143
	v_fma_f32 v144, v176, v144, v134
	v_fma_f32 v145, v177, v145, v135
	v_fma_f32 v140, v174, v154, v136
	v_fma_f32 v141, v175, v155, v137
	v_fma_f32 v134, v246, v144, v244
	v_fma_f32 v135, v247, v145, v245
	v_fma_f32 v136, v156, v140, v242
	v_fma_f32 v137, v157, v141, v243
	s_and_saveexec_b64 s[42:43], s[16:17]
	s_cbranch_execz .LBB1_143
	v_mov_b32_e32 v115, s56
	v_cndmask_b32_e64 v115, v137, v115, s[14:15]
	v_cndmask_b32_e64 v147, v136, v136, s[14:15]
	v_cndmask_b32_e64 v146, v135, v135, s[14:15]
	v_cndmask_b32_e64 v148, v134, v134, s[14:15]
	v_cvt_pk_bf16_f32 v146, v148, v146
	v_cvt_pk_bf16_f32 v147, v147, v115
	v_mad_u32_u24 v115, v236, s53, v204
	ds_write_b64 v115, v[146:147]

.Lpoll_done_3:
	ds_read_b128 v[142:145], v202 offset:58112
	ds_read_b128 v[146:149], v202 offset:58176
	v_mul_f32_e32 v238, v172, v152
	v_mul_f32_e32 v239, v173, v153
	v_mul_f32_e32 v240, v174, v150
	v_mul_f32_e32 v241, v175, v151
	s_waitcnt lgkmcnt(1)
	v_mfma_f32_16x16x32_bf16 v[134:137], v[134:137], v[142:145], 0
	v_add_f32_e64 v242, -v174, 1.0
	v_add_f32_e64 v243, -v175, 1.0
	s_waitcnt lgkmcnt(0)
	v_sub_f32_e32 v144, 1.0, v234
	v_sub_f32_e32 v145, 1.0, v235
	v_mfma_f32_16x16x32_bf16 v[140:143], v[138:141], v[146:149], 0
	v_sub_f32_e32 v154, 1.0, v236
	v_sub_f32_e32 v155, 1.0, v237
	v_sub_f32_e32 v156, 1.0, v172
	v_sub_f32_e32 v157, 1.0, v173
	v_sub_f32_e32 v158, v150, v176
	v_sub_f32_e32 v159, v151, v177
	v_sub_f32_e32 v160, v152, v116
	v_sub_f32_e32 v161, v153, v117
	v_add_f32_e32 v138, v136, v142
	v_add_f32_e32 v139, v137, v143
	v_add_f32_e32 v142, v134, v140
	v_add_f32_e32 v143, v135, v141
	v_mul_f32_e32 v136, v236, v138
	v_mul_f32_e32 v137, v237, v139
	v_mul_f32_e32 v134, v234, v142
	v_mul_f32_e32 v135, v235, v143
	v_fma_f32 v144, v176, v144, v134
	v_fma_f32 v145, v177, v145, v135
	v_fma_f32 v140, v116, v154, v136
	v_fma_f32 v141, v117, v155, v137
	v_fma_f32 v134, v242, v144, v240
	v_fma_f32 v135, v243, v145, v241
	v_fma_f32 v136, v156, v140, v238
	v_fma_f32 v137, v157, v141, v239
	s_and_saveexec_b64 s[44:45], s[16:17]
	s_cbranch_execz .LBB1_183
	v_mov_b32_e32 v115, s56
	v_cndmask_b32_e64 v115, v137, v115, s[14:15]
	v_cndmask_b32_e64 v147, v136, v136, s[14:15]
	v_cndmask_b32_e64 v146, v135, v135, s[14:15]
	v_cndmask_b32_e64 v148, v134, v134, s[14:15]
	v_cvt_pk_bf16_f32 v146, v148, v146
	v_cvt_pk_bf16_f32 v147, v147, v115
	v_mad_u32_u24 v115, v167, s53, v204
	ds_write_b64 v115, v[146:147]

.LBB1_189:
	s_or_b64 exec, exec, s[44:45]
	v_sub_f32_e32 v134, v150, v142
	v_add_f32_e64 v115, |v158|, |v134|
	v_sub_f32_e32 v134, v150, v144
	v_sub_f32_e32 v136, v151, v143
	v_add_f32_e64 v115, v115, |v134|
	v_add_f32_e64 v135, |v159|, |v136|
	v_sub_f32_e32 v136, v151, v145
	v_fma_f32 v115, v174, v115, 0
	v_add_f32_e64 v135, v135, |v136|
	v_fmac_f32_e32 v115, v175, v135
	v_sub_f32_e32 v135, v152, v138
	v_add_f32_e32 v134, 0, v174
	v_add_f32_e64 v116, |v160|, |v135|
	v_sub_f32_e32 v135, v152, v140
	v_add_f32_e32 v134, v175, v134
	v_add_f32_e64 v116, v116, |v135|
	v_fmac_f32_e32 v115, v172, v116
	v_add_f32_e32 v116, v172, v134
	v_sub_f32_e32 v134, v153, v139
	v_add_f32_e64 v117, |v161|, |v134|
	v_sub_f32_e32 v134, v153, v141
	v_add_f32_e64 v117, v117, |v134|
	v_fmac_f32_e32 v115, v173, v117
	v_add_f32_e32 v116, v173, v116
	s_nop 0
	v_mov_b32_e32 v246, v115
	v_mov_b32_e32 v247, v116
